# stack10 + attention tile loop: one static s_setprio 1 for waves 4-7 (younger half), reset at the unit tail
# baseline (speedup 1.0000x reference)
; #define LAS __attribute__((address_space(3)))
; __device__ __forceinline__ float half_swap_max(float m) { unsigned a = __builtin_bit_cast(unsigned, m), b = a; half_swap(a, b); return __builtin_fmaxf(__builtin_bit_cast(float, a), __builtin_bit_cast(float, b)); }
; #define EX2(P, i) do { P[i] = __builtin_amdgcn_exp2f(P[i]); P[(i) + 1] = __builtin_amdgcn_exp2f(P[(i) + 1]); } while (0)
; #define PK8(P, i) ({ v4u w_; w_.x = pk2(P[i], P[(i) + 1]); w_.y = pk2(P[(i) + 2], P[(i) + 3]); w_.z = pk2(P[(i) + 4], P[(i) + 5]); w_.w = pk2(P[(i) + 6], P[(i) + 7]); __builtin_bit_cast(bf16x8, w_); })
; __device__ __forceinline__ void attn_unit(LAS unsigned char* lds, const bf16* proj, bf16* Y, const float* relb, const float* hgain, float lam, float oscale, int b, int h, int qb, int tid, int lane, int wid, Stopwatch& sw) {
;     ...
;       float mt = __builtin_fmaxf(sA0[0], sA1[0]);
; #pragma unroll
;       for (int r = 1; r < 16; ++r) mt = __builtin_fmaxf(mt, __builtin_fmaxf(sA0[r], sA1[r]));
;       mt = half_swap_max(mt); m_run = mt;
; #pragma unroll
;       for (int r = 0; r < 16; ++r) { sA0[r] -= mt; sA1[r] -= mt; } }
;     int sc = 0, sn = 32768, sn2 = 65536;
;     ...
;     bf16x8 qreg[4];
; #pragma unroll
;     for (int d0 = 0; d0 < 4; ++d0) qreg[d0] = *(const LAS bf16x8*)(qlds + d0 * 1024);
;     bf16x8 pw0, pw1, pw2, pw3;
;     {
; #pragma unroll
;       for (int r = 0; r < 16; r += 2) { EX2(sA0, r); EX2(sA1, r); }
;       float sm_ = 0.f;
; #pragma unroll
;       for (int r = 0; r < 16; ++r) sm_ += sA0[r] + sA1[r];
;       l_run += sm_; pw0 = PK8(sA0, 0); pw1 = PK8(sA0, 8); pw2 = PK8(sA1, 0); pw3 = PK8(sA1, 8); }
.LBB0_394:
	v_and_b32_e32 v166, 63, v61
	v_lshrrev_b32_e32 v36, 2, v61
	v_lshlrev_b32_e32 v41, 3, v166
	v_and_b32_e32 v36, 11, v36
	v_lshrrev_b32_e32 v37, 3, v61
	v_and_b32_e32 v38, 1, v63
	v_and_b32_e32 v41, 8, v41
	v_and_or_b32 v37, v37, 2, v38
	v_lshrrev_b32_e32 v39, 2, v36
	v_lshl_or_b32 v42, v36, 8, v41
	v_or_b32_e32 v36, 4, v36
	v_and_b32_e32 v38, 12, v61
	v_lshrrev_b32_e32 v43, 2, v36
	v_lshl_or_b32 v41, v36, 8, v41
	v_or_b32_e32 v36, 4, v37
	v_bitop3_b32 v46, v43, v36, v38 bitop3:0x36
	v_or_b32_e32 v36, 8, v37
	v_or_b32_e32 v40, v39, v38
	v_bitop3_b32 v48, v43, v36, v38 bitop3:0x36
	v_or_b32_e32 v36, 12, v37
	v_bitop3_b32 v39, v39, v37, v38 bitop3:0x36
	v_bitop3_b32 v44, v43, v37, v38 bitop3:0x36
	v_bitop3_b32 v45, v37, v40, 4 bitop3:0x36
	v_bitop3_b32 v47, v37, v40, 8 bitop3:0x36
	v_bitop3_b32 v40, v37, v40, 12 bitop3:0x36
	v_bitop3_b32 v38, v43, v36, v38 bitop3:0x36
	v_max_f32_e32 v36, v5, v5
	v_max_f32_e32 v37, v21, v21
	v_max_f32_e32 v36, v37, v36
	v_max_f32_e32 v37, v6, v6
	v_max_f32_e32 v43, v22, v22
	v_max_f32_e32 v37, v43, v37
	v_max_f32_e32 v43, v7, v7
	v_max_f32_e32 v49, v23, v23
	v_max3_f32 v36, v20, v4, v36
	v_max_f32_e32 v43, v49, v43
	v_max3_f32 v36, v36, v37, v43
	v_max_f32_e32 v37, v8, v8
	v_max_f32_e32 v43, v24, v24
	v_max_f32_e32 v37, v43, v37
	v_max_f32_e32 v43, v9, v9
	v_max_f32_e32 v49, v25, v25
	v_max_f32_e32 v43, v49, v43
	v_max3_f32 v36, v36, v37, v43
	v_max_f32_e32 v37, v10, v10
	v_max_f32_e32 v43, v26, v26
	v_max_f32_e32 v37, v43, v37
	v_max_f32_e32 v43, v11, v11
	v_max_f32_e32 v49, v27, v27
	v_max_f32_e32 v43, v49, v43
	v_max3_f32 v36, v36, v37, v43
	v_max_f32_e32 v37, v12, v12
	v_max_f32_e32 v43, v28, v28
	v_max_f32_e32 v37, v43, v37
	v_max_f32_e32 v43, v13, v13
	v_max_f32_e32 v49, v29, v29
	v_max_f32_e32 v43, v49, v43
	v_max3_f32 v36, v36, v37, v43
	v_max_f32_e32 v37, v14, v14
	v_max_f32_e32 v43, v30, v30
	v_max_f32_e32 v37, v43, v37
	v_max_f32_e32 v43, v15, v15
	v_max_f32_e32 v49, v31, v31
	v_max_f32_e32 v43, v49, v43
	v_max3_f32 v36, v36, v37, v43
	v_max_f32_e32 v37, v16, v16
	v_max_f32_e32 v43, v32, v32
	v_max_f32_e32 v37, v43, v37
	v_max_f32_e32 v43, v17, v17
	v_max_f32_e32 v49, v33, v33
	v_max_f32_e32 v43, v49, v43
	v_max3_f32 v36, v36, v37, v43
	v_max_f32_e32 v37, v18, v18
	v_max_f32_e32 v43, v34, v34
	v_max_f32_e32 v37, v43, v37
	v_max_f32_e32 v43, v19, v19
	v_max_f32_e32 v49, v35, v35
	v_max_f32_e32 v43, v49, v43
	v_max3_f32 v36, v36, v37, v43
	v_mov_b32_e32 v37, v36
	s_nop 1
	v_permlane32_swap_b32 v36, v37
	s_nop 1
	ds_read_b128 v[116:119], v62
	ds_read_b128 v[120:123], v62 offset:1024
	ds_read_b128 v[124:127], v62 offset:2048
	ds_read_b128 v[128:131], v62 offset:3072
	v_max_f32_e32 v37, v37, v37
	v_max_f32_e32 v36, v36, v36
	v_max_f32_e32 v167, v36, v37
	v_sub_f32_e32 v20, v20, v167
	v_sub_f32_e32 v36, v4, v167
	v_sub_f32_e32 v4, v21, v167
	v_sub_f32_e32 v5, v5, v167
	v_exp_f32_e32 v62, v20
	v_exp_f32_e32 v63, v36
	v_sub_f32_e32 v21, v22, v167
	v_sub_f32_e32 v22, v6, v167
	v_exp_f32_e32 v4, v4
	v_exp_f32_e32 v6, v5
	v_sub_f32_e32 v23, v23, v167
	v_sub_f32_e32 v7, v7, v167
	v_exp_f32_e32 v64, v21
	v_exp_f32_e32 v65, v22
	v_sub_f32_e32 v37, v8, v167
	v_sub_f32_e32 v43, v10, v167
	v_exp_f32_e32 v8, v23
	v_exp_f32_e32 v10, v7
	v_add_f32_e32 v5, v62, v63
	v_mov_b32_e32 v7, v3
	v_sub_f32_e32 v24, v24, v167
	v_exp_f32_e32 v67, v37
	v_pk_add_f32 v[36:37], v[4:5], v[6:7]
	v_sub_f32_e32 v25, v25, v167
	v_sub_f32_e32 v9, v9, v167
	v_sub_f32_e32 v11, v11, v167
	v_exp_f32_e32 v66, v24
	v_pk_add_f32 v[36:37], v[36:37], v[36:37] op_sel_hi:[0,1]
	v_sub_f32_e32 v49, v12, v167
	v_sub_f32_e32 v50, v14, v167
	v_sub_f32_e32 v61, v18, v167
	v_exp_f32_e32 v12, v25
	v_exp_f32_e32 v14, v9
	v_exp_f32_e32 v18, v11
	v_add_f32_e32 v9, v64, v65
	v_mov_b32_e32 v11, v37
	v_sub_f32_e32 v26, v26, v167
	v_pk_add_f32 v[36:37], v[8:9], v[10:11]
	v_sub_f32_e32 v27, v27, v167
	v_sub_f32_e32 v13, v13, v167
	v_sub_f32_e32 v15, v15, v167
	v_exp_f32_e32 v68, v26
	v_exp_f32_e32 v43, v43
	v_pk_add_f32 v[36:37], v[36:37], v[36:37] op_sel_hi:[0,1]
	v_sub_f32_e32 v51, v16, v167
	v_exp_f32_e32 v16, v27
	v_exp_f32_e32 v22, v13
	v_exp_f32_e32 v26, v15
	v_add_f32_e32 v13, v66, v67
	v_mov_b32_e32 v15, v37
	v_sub_f32_e32 v28, v28, v167
; #define EX2(P, i) do { P[i] = __builtin_amdgcn_exp2f(P[i]); P[(i) + 1] = __builtin_amdgcn_exp2f(P[(i) + 1]); } while (0)
; #define PK8(P, i) ({ v4u w_; w_.x = pk2(P[i], P[(i) + 1]); w_.y = pk2(P[(i) + 2], P[(i) + 3]); w_.z = pk2(P[(i) + 4], P[(i) + 5]); w_.w = pk2(P[(i) + 6], P[(i) + 7]); __builtin_bit_cast(bf16x8, w_); })
; __device__ __forceinline__ void attn_unit(LAS unsigned char* lds, const bf16* proj, bf16* Y, const float* relb, const float* hgain, float lam, float oscale, int b, int h, int qb, int tid, int lane, int wid, Stopwatch& sw) {
;     ...
;     bf16x8 pw0, pw1, pw2, pw3;
;     {
; #pragma unroll
;       for (int r = 0; r < 16; r += 2) { EX2(sA0, r); EX2(sA1, r); }
;       float sm_ = 0.f;
; #pragma unroll
;       for (int r = 0; r < 16; ++r) sm_ += sA0[r] + sA1[r];
;       l_run += sm_; pw0 = PK8(sA0, 0); pw1 = PK8(sA0, 8); pw2 = PK8(sA1, 0); pw3 = PK8(sA1, 8); }
	v_pk_add_f32 v[36:37], v[12:13], v[14:15]
	v_sub_f32_e32 v29, v29, v167
	v_sub_f32_e32 v30, v30, v167
	v_sub_f32_e32 v17, v17, v167
	v_sub_f32_e32 v34, v34, v167
	v_sub_f32_e32 v19, v19, v167
	v_exp_f32_e32 v69, v28
	v_exp_f32_e32 v49, v49
	v_pk_add_f32 v[36:37], v[36:37], v[36:37] op_sel_hi:[0,1]
	v_exp_f32_e32 v20, v29
	v_exp_f32_e32 v70, v30
	v_exp_f32_e32 v30, v17
	v_exp_f32_e32 v72, v34
	v_exp_f32_e32 v34, v19
	v_add_f32_e32 v17, v68, v43
	v_mov_b32_e32 v19, v37
	v_pk_add_f32 v[36:37], v[16:17], v[18:19]
	v_sub_f32_e32 v31, v31, v167
	v_exp_f32_e32 v50, v50
	v_pk_add_f32 v[36:37], v[36:37], v[36:37] op_sel_hi:[0,1]
	v_exp_f32_e32 v24, v31
	v_add_f32_e32 v21, v69, v49
	v_mov_b32_e32 v23, v37
	v_sub_f32_e32 v32, v32, v167
	v_pk_add_f32 v[36:37], v[20:21], v[22:23]
	v_sub_f32_e32 v33, v33, v167
	v_exp_f32_e32 v71, v32
	v_exp_f32_e32 v51, v51
	v_pk_add_f32 v[36:37], v[36:37], v[36:37] op_sel_hi:[0,1]
	v_exp_f32_e32 v28, v33
	v_add_f32_e32 v25, v70, v50
	v_mov_b32_e32 v27, v37
	v_pk_add_f32 v[36:37], v[24:25], v[26:27]
	v_sub_f32_e32 v35, v35, v167
	v_exp_f32_e32 v61, v61
	v_pk_add_f32 v[36:37], v[36:37], v[36:37] op_sel_hi:[0,1]
	v_exp_f32_e32 v32, v35
	v_add_f32_e32 v29, v71, v51
	v_mov_b32_e32 v31, v37
	v_pk_add_f32 v[36:37], v[28:29], v[30:31]
	v_add_f32_e32 v33, v72, v61
	v_pk_add_f32 v[36:37], v[36:37], v[36:37] op_sel_hi:[0,1]
	v_mov_b32_e32 v35, v37
	s_lshl_b32 s18, s0, 7
	v_pk_add_f32 v[36:37], v[32:33], v[34:35]
	s_mov_b64 s[36:37], 0x380000
	v_readlane_b32 s0, v252, 60
	v_add_f32_e32 v5, v36, v37
	v_cvt_pk_bf16_f32 v144, v62, v4
	v_lshl_add_u64 v[160:161], v[52:53], 0, s[36:37]
	v_add_u32_e32 v4, s0, v60
	v_mov_b32_e32 v52, v3
	v_mov_b32_e32 v53, v3
	v_add_f32_e32 v153, 0, v5
	v_cvt_pk_bf16_f32 v145, v64, v8
	v_cvt_pk_bf16_f32 v146, v66, v12
	v_cvt_pk_bf16_f32 v147, v68, v16
	v_cvt_pk_bf16_f32 v140, v69, v20
	v_cvt_pk_bf16_f32 v141, v70, v24
	v_cvt_pk_bf16_f32 v142, v71, v28
	v_cvt_pk_bf16_f32 v143, v72, v32
	v_cvt_pk_bf16_f32 v132, v63, v6
	v_cvt_pk_bf16_f32 v133, v65, v10
	v_cvt_pk_bf16_f32 v134, v67, v14
	v_cvt_pk_bf16_f32 v135, v43, v18
	v_cvt_pk_bf16_f32 v136, v49, v22
	v_cvt_pk_bf16_f32 v137, v50, v26
	v_cvt_pk_bf16_f32 v138, v51, v30
	v_cvt_pk_bf16_f32 v139, v61, v34
	v_lshl_or_b32 v175, v39, 4, v42
	v_lshl_or_b32 v174, v44, 4, v41
	v_lshl_or_b32 v173, v45, 4, v42
	v_lshl_or_b32 v172, v46, 4, v41
	v_lshl_or_b32 v171, v47, 4, v42
	v_lshl_or_b32 v170, v48, 4, v41
	v_lshl_or_b32 v169, v40, 4, v42
	v_lshl_or_b32 v168, v38, 4, v41
	v_lshl_add_u64 v[154:155], v[58:59], 0, s[36:37]
	v_lshl_add_u64 v[156:157], v[54:55], 0, s[36:37]
	v_lshl_add_u64 v[158:159], v[56:57], 0, s[36:37]
	v_sub_u32_e32 v176, v4, v150
	v_mov_b32_e32 v54, v3
	v_mov_b32_e32 v55, v3
	v_mov_b32_e32 v56, v3
	v_mov_b32_e32 v57, v3
	v_mov_b32_e32 v58, v3
	v_mov_b32_e32 v59, v3
	v_mov_b32_e32 v60, v3
	v_mov_b32_e32 v61, v3
	v_mov_b32_e32 v62, v3
	v_mov_b32_e32 v63, v3
	v_mov_b32_e32 v64, v3
	v_mov_b32_e32 v65, v3
	v_mov_b32_e32 v66, v3
	v_mov_b32_e32 v67, v3
	v_mov_b64_e32 v[36:37], v[52:53]
	v_mov_b64_e32 v[20:21], v[52:53]
	v_mov_b64_e32 v[4:5], v[52:53]
	s_lshl_b32 s19, s19, 1
	s_or_b32 s24, s16, 31
	s_mov_b32 s25, 0x10000
	s_mov_b32 s31, 0x8000
	s_mov_b32 s0, 0
	s_movk_i32 s34, 0xffc0
	v_mov_b64_e32 v[38:39], v[54:55]
	v_mov_b64_e32 v[40:41], v[56:57]
	v_mov_b64_e32 v[42:43], v[58:59]
	v_mov_b64_e32 v[44:45], v[60:61]
	v_mov_b64_e32 v[46:47], v[62:63]
	v_mov_b64_e32 v[48:49], v[64:65]
	v_mov_b64_e32 v[50:51], v[66:67]
	v_mov_b64_e32 v[22:23], v[54:55]
	v_mov_b64_e32 v[24:25], v[56:57]
	v_mov_b64_e32 v[26:27], v[58:59]
	v_mov_b64_e32 v[28:29], v[60:61]
	v_mov_b64_e32 v[30:31], v[62:63]
	v_mov_b64_e32 v[32:33], v[64:65]
	v_mov_b64_e32 v[34:35], v[66:67]
	v_mov_b64_e32 v[6:7], v[54:55]
	v_mov_b64_e32 v[8:9], v[56:57]
	v_mov_b64_e32 v[10:11], v[58:59]
	v_mov_b64_e32 v[12:13], v[60:61]
	v_mov_b64_e32 v[14:15], v[62:63]
	v_mov_b64_e32 v[16:17], v[64:65]
	v_mov_b64_e32 v[18:19], v[66:67]
	v_readfirstlane_b32 s101, v1
	s_nop 3
	s_bfe_u32 s101, s101, 0x10008
	s_cmp_eq_u32 s101, 0
	s_cbranch_scc1 .Latt_prio_done
	s_setprio 1
.Latt_prio_done:
	s_mov_b32 s72, 0
	s_cmp_ge_u32 s72, s19
	s_mov_b32 s73, s0
	s_cbranch_scc1 .LBB0_397
	s_branch .LBB0_396

; #define LAS __attribute__((address_space(3)))
; __device__ __forceinline__ float half_swap_sum(float m) { unsigned a = __builtin_bit_cast(unsigned, m), b = a; half_swap(a, b); return __builtin_bit_cast(float, a) + __builtin_bit_cast(float, b); }
; __device__ __forceinline__ void attn_unit(LAS unsigned char* lds, const bf16* proj, bf16* Y, const float* relb, const float* hgain, float lam, float oscale, int b, int h, int qb, int tid, int lane, int wid, Stopwatch& sw) {
;     ...
;     l_run = half_swap_sum(l_run);
;     const float inv = 1.f / l_run;
;     LAS float* xch = (LAS float*)lds;
;     if (mp == 1) {
; #pragma unroll
;         for (int c = 0; c < 4; ++c)
; #pragma unroll
;             for (int r = 0; r < 16; ++r) xch[((wq * 64 + c * 16 + r) << 6) + lane] = o[c][r] * inv;
;     }
.LBB0_442:
	s_setprio 0
	v_mov_b32_e32 v68, v153
	s_waitcnt vmcnt(0) lgkmcnt(0)
	s_barrier
	s_nop 1
	v_permlane32_swap_b32 v153, v68
	s_nop 1
	v_readlane_b32 s72, v255, 20
	v_add_f32_e32 v68, v153, v68
	v_div_scale_f32 v69, s[24:25], v68, v68, 1.0
	v_rcp_f32_e32 v70, v69
	v_readlane_b32 s24, v253, 7
	v_readlane_b32 s25, v253, 8
	v_readlane_b32 s73, v255, 21
	v_fma_f32 v71, -v69, v70, 1.0
	v_fmac_f32_e32 v70, v71, v70
	v_div_scale_f32 v71, vcc, 1.0, v68, 1.0
	v_mul_f32_e32 v72, v71, v70
	v_fma_f32 v73, -v69, v72, v71
	v_fmac_f32_e32 v72, v73, v70
	v_fma_f32 v69, -v69, v72, v71
	v_div_fmas_f32 v69, v69, v70, v72
	v_readlane_b32 s31, v255, 25
	s_mov_b32 s69, 0x10000
	s_mov_b32 s82, 0xf800000
	s_mov_b32 s16, 0x30000
	s_andn2_b64 vcc, exec, s[24:25]
	v_div_fixup_f32 v80, v69, v68, 1.0
	s_cbranch_vccnz .LBB0_444
	v_readlane_b32 s0, v253, 10
	v_mul_f32_e32 v68, v52, v80
	v_mul_f32_e32 v70, v53, v80
	v_lshl_add_u32 v69, v166, 2, s0
	ds_write2st64_b32 v69, v68, v70 offset1:1
	v_mul_f32_e32 v68, v54, v80
	v_mul_f32_e32 v70, v55, v80
	ds_write2st64_b32 v69, v68, v70 offset0:2 offset1:3
	v_mul_f32_e32 v68, v56, v80
	v_mul_f32_e32 v70, v57, v80
	ds_write2st64_b32 v69, v68, v70 offset0:4 offset1:5
	v_mul_f32_e32 v68, v58, v80
	v_mul_f32_e32 v70, v59, v80
	ds_write2st64_b32 v69, v68, v70 offset0:6 offset1:7
	v_mul_f32_e32 v68, v60, v80
	v_mul_f32_e32 v70, v61, v80
	ds_write2st64_b32 v69, v68, v70 offset0:8 offset1:9
	v_mul_f32_e32 v68, v62, v80
	v_mul_f32_e32 v70, v63, v80
	ds_write2st64_b32 v69, v68, v70 offset0:10 offset1:11
	v_mul_f32_e32 v68, v64, v80
	v_mul_f32_e32 v70, v65, v80
	ds_write2st64_b32 v69, v68, v70 offset0:12 offset1:13
	v_mul_f32_e32 v68, v66, v80
	v_mul_f32_e32 v70, v67, v80
	ds_write2st64_b32 v69, v68, v70 offset0:14 offset1:15
	v_mul_f32_e32 v68, v36, v80
	v_mul_f32_e32 v70, v37, v80
	ds_write2st64_b32 v69, v68, v70 offset0:16 offset1:17
	v_mul_f32_e32 v68, v38, v80
	v_mul_f32_e32 v70, v39, v80
	ds_write2st64_b32 v69, v68, v70 offset0:18 offset1:19
	v_mul_f32_e32 v68, v40, v80
	v_mul_f32_e32 v70, v41, v80
	ds_write2st64_b32 v69, v68, v70 offset0:20 offset1:21
	v_mul_f32_e32 v68, v42, v80
	v_mul_f32_e32 v70, v43, v80
	ds_write2st64_b32 v69, v68, v70 offset0:22 offset1:23
	v_mul_f32_e32 v68, v44, v80
	v_mul_f32_e32 v70, v45, v80
	ds_write2st64_b32 v69, v68, v70 offset0:24 offset1:25
	v_mul_f32_e32 v68, v46, v80
	v_mul_f32_e32 v70, v47, v80
	ds_write2st64_b32 v69, v68, v70 offset0:26 offset1:27
	v_mul_f32_e32 v68, v48, v80
	v_mul_f32_e32 v70, v49, v80
	ds_write2st64_b32 v69, v68, v70 offset0:28 offset1:29
	v_mul_f32_e32 v68, v50, v80
	v_mul_f32_e32 v70, v51, v80
	ds_write2st64_b32 v69, v68, v70 offset0:30 offset1:31
	v_mul_f32_e32 v68, v20, v80
	v_mul_f32_e32 v70, v21, v80
	ds_write2st64_b32 v69, v68, v70 offset0:32 offset1:33
	v_mul_f32_e32 v68, v22, v80
	v_mul_f32_e32 v70, v23, v80
	ds_write2st64_b32 v69, v68, v70 offset0:34 offset1:35
	v_mul_f32_e32 v68, v24, v80
	v_mul_f32_e32 v70, v25, v80
	ds_write2st64_b32 v69, v68, v70 offset0:36 offset1:37
	v_mul_f32_e32 v68, v26, v80
	v_mul_f32_e32 v70, v27, v80
	ds_write2st64_b32 v69, v68, v70 offset0:38 offset1:39
	v_mul_f32_e32 v68, v28, v80
	v_mul_f32_e32 v70, v29, v80
	ds_write2st64_b32 v69, v68, v70 offset0:40 offset1:41
	v_mul_f32_e32 v68, v30, v80
	v_mul_f32_e32 v70, v31, v80
	ds_write2st64_b32 v69, v68, v70 offset0:42 offset1:43
	v_mul_f32_e32 v68, v32, v80
	v_mul_f32_e32 v70, v33, v80
	ds_write2st64_b32 v69, v68, v70 offset0:44 offset1:45
	v_mul_f32_e32 v68, v34, v80
	v_mul_f32_e32 v70, v35, v80
	ds_write2st64_b32 v69, v68, v70 offset0:46 offset1:47
	v_mul_f32_e32 v68, v4, v80
	v_mul_f32_e32 v70, v5, v80
	ds_write2st64_b32 v69, v68, v70 offset0:48 offset1:49
	v_mul_f32_e32 v68, v6, v80
	v_mul_f32_e32 v70, v7, v80
	ds_write2st64_b32 v69, v68, v70 offset0:50 offset1:51
	v_mul_f32_e32 v68, v8, v80
	v_mul_f32_e32 v70, v9, v80
	ds_write2st64_b32 v69, v68, v70 offset0:52 offset1:53
	v_mul_f32_e32 v68, v10, v80
	v_mul_f32_e32 v70, v11, v80
	ds_write2st64_b32 v69, v68, v70 offset0:54 offset1:55
	v_mul_f32_e32 v68, v12, v80
	v_mul_f32_e32 v70, v13, v80
	ds_write2st64_b32 v69, v68, v70 offset0:56 offset1:57
	v_mul_f32_e32 v68, v14, v80
	v_mul_f32_e32 v70, v15, v80
	ds_write2st64_b32 v69, v68, v70 offset0:58 offset1:59
	v_mul_f32_e32 v68, v16, v80
	v_mul_f32_e32 v70, v17, v80
	ds_write2st64_b32 v69, v68, v70 offset0:60 offset1:61
	v_mul_f32_e32 v68, v18, v80
	v_mul_f32_e32 v70, v19, v80
	ds_write2st64_b32 v69, v68, v70 offset0:62 offset1:63
